# MoE grouped GEMM phases P8/P9: workgroup id permuted so the 4 WGs sharing an A row tile sit on one XCD (bid%8)
# speedup vs baseline: 1.0102x; 1.0102x over previous
.LBB0_797:
	s_mov_b32 s98, s30
	s_and_b32 s99, s30, 7
	s_lshl_b32 s99, s99, 5
	s_lshr_b32 s30, s30, 3
	s_or_b32 s30, s30, s99
	s_lshl_b32 s99, s30, 3
	s_nop 0
	v_writelane_b32 v253, s99, 19
	s_cmp_lt_i32 s90, 9
	s_cselect_b64 s[0:1], -1, 0
	s_and_b64 s[2:3], s[0:1], s[2:3]
	s_andn2_b64 vcc, exec, s[2:3]
	s_cbranch_vccnz .LBB0_863
	v_mov_b32_e32 v0, 0x780000
	global_load_dword v0, v0, s[88:89] offset:1200 sc1
	s_add_u32 s4, s88, 0x7804b0
	s_addc_u32 s5, s89, 0
	s_add_i32 s8, s76, s30
	s_add_i32 s10, s8, s76
	s_add_i32 s12, s10, s76
	s_add_i32 s14, s12, s76
	s_add_i32 s16, s14, s76
	s_ashr_i32 s70, s30, 2
	s_ashr_i32 s9, s8, 2
	s_ashr_i32 s11, s10, 2
	s_ashr_i32 s13, s12, 2
	s_ashr_i32 s15, s14, 2
	s_ashr_i32 s17, s16, 2
	v_mov_b32_e32 v193, 0
	s_waitcnt vmcnt(37)
	v_lshlrev_b32_e32 v6, 4, v236
	v_and_b32_e32 v7, 32, v236
	s_waitcnt vmcnt(7)
	v_lshrrev_b32_e32 v10, 1, v236
	v_lshlrev_b32_e32 v11, 6, v236
	s_waitcnt vmcnt(2)
	v_lshlrev_b32_e32 v12, 2, v236
	v_lshrrev_b32_e32 v13, 5, v236
	v_bfe_u32 v14, v236, 2, 2
	v_bitop3_b32 v7, v6, v7, 48 bitop3:0x6c
	v_add_u32_e32 v6, 0x2000, v6
	v_and_b32_e32 v239, 24, v10
	v_and_b32_e32 v10, 0x3c0, v11
	v_and_b32_e32 v11, 32, v12
	v_and_b32_e32 v12, 4, v13
	v_bfe_u32 v8, v236, 2, 4
	v_lshrrev_b32_e32 v9, 3, v236
	v_and_or_b32 v243, v236, 64, v7
	v_lshrrev_b32_e32 v6, 7, v6
	v_lshlrev_b32_e32 v241, 1, v239
	v_or3_b32 v7, v12, v14, v239
	v_and_b32_e32 v238, 15, v236
	v_bitop3_b32 v240, v241, v11, v10 bitop3:0x36
	s_waitcnt vmcnt(0)
	v_readfirstlane_b32 s2, v0
	s_lshl_b32 s31, s2, 2
	s_cmp_lt_i32 s30, s31
	s_cselect_b32 s2, s70, 0
	s_ashr_i32 s3, s2, 31
	s_lshl_b64 s[2:3], s[2:3], 2
	s_add_u32 s2, s6, s2
	s_addc_u32 s3, s7, s3
	s_cmp_lt_i32 s8, s31
	global_load_dword v0, v193, s[2:3] sc1
	s_cselect_b32 s2, s9, 0
	s_ashr_i32 s3, s2, 31
	s_lshl_b64 s[2:3], s[2:3], 2
	s_add_u32 s2, s6, s2
	s_addc_u32 s3, s7, s3
	s_cmp_lt_i32 s10, s31
	global_load_dword v1, v193, s[2:3] sc1
	s_cselect_b32 s2, s11, 0
	s_ashr_i32 s3, s2, 31
	s_lshl_b64 s[2:3], s[2:3], 2
	s_add_u32 s2, s6, s2
	s_addc_u32 s3, s7, s3
	s_cmp_lt_i32 s12, s31
	global_load_dword v2, v193, s[2:3] sc1
	s_cselect_b32 s2, s13, 0
	s_ashr_i32 s3, s2, 31
	s_lshl_b64 s[2:3], s[2:3], 2
	s_add_u32 s2, s6, s2
	s_addc_u32 s3, s7, s3
	s_cmp_lt_i32 s14, s31
	global_load_dword v3, v193, s[2:3] sc1
	s_cselect_b32 s2, s15, 0
	s_ashr_i32 s3, s2, 31
	s_lshl_b64 s[2:3], s[2:3], 2
	s_add_u32 s2, s6, s2
	s_addc_u32 s3, s7, s3
	s_cmp_lt_i32 s16, s31
	global_load_dword v4, v193, s[2:3] sc1
	s_cselect_b32 s2, s17, 0
	s_ashr_i32 s3, s2, 31
	s_lshl_b64 s[2:3], s[2:3], 2
	s_add_u32 s2, s6, s2
	s_addc_u32 s3, s7, s3
	global_load_dword v5, v193, s[2:3] sc1
	s_movk_i32 s2, 0x70
	s_movk_i32 s3, 0xf0
	s_movk_i32 s8, 0xe0
	s_movk_i32 s9, 0x60
	v_and_or_b32 v242, v9, s2, v8
	v_and_or_b32 v244, v6, s3, v8
	v_and_or_b32 v245, v6, s8, v7
	v_and_or_b32 v246, v9, s9, v7
	s_cmp_ge_i32 s30, s31
	v_readfirstlane_b32 s2, v236
	s_waitcnt vmcnt(5)
	v_readfirstlane_b32 s10, v0
	s_waitcnt vmcnt(4)
	v_readfirstlane_b32 s33, v1
	s_waitcnt vmcnt(3)
	v_readfirstlane_b32 s50, v2
	s_waitcnt vmcnt(2)
	v_readfirstlane_b32 s51, v3
	s_waitcnt vmcnt(1)
	v_readfirstlane_b32 s52, v4
	s_waitcnt vmcnt(0)
	v_readfirstlane_b32 s53, v5
	s_cbranch_scc1 .LBB0_844
	s_add_u32 s8, s88, 0x7a0000
	s_addc_u32 s9, s89, 0
	s_lshl_b32 s3, s70, 8
	s_or_b32 s11, s3, 0x80
	v_or_b32_e32 v6, s3, v242
	v_add_u32_e32 v0, s11, v244
	v_or_b32_e32 v2, s11, v242
	v_or_b32_e32 v4, s3, v244
	v_ashrrev_i32_e32 v7, 31, v6
	v_ashrrev_i32_e32 v1, 31, v0
	v_ashrrev_i32_e32 v3, 31, v2
	v_ashrrev_i32_e32 v5, 31, v4
	v_lshl_add_u64 v[6:7], v[6:7], 2, s[8:9]
	v_lshl_add_u64 v[0:1], v[0:1], 2, s[8:9]
	v_lshl_add_u64 v[2:3], v[2:3], 2, s[8:9]
	v_lshl_add_u64 v[4:5], v[4:5], 2, s[8:9]
	global_load_dword v8, v[6:7], off
	global_load_dword v9, v[4:5], off
	global_load_dword v10, v[2:3], off
	global_load_dword v11, v[0:1], off
	s_and_b32 s11, s30, 3
	s_lshl_b32 s10, s10, 2
	s_or_b32 s44, s10, s11
	s_lshr_b32 s18, s2, 6
	s_ashr_i32 s45, s44, 31
	s_lshr_b32 s3, s2, 8
	s_lshl_b32 s54, s18, 10
	s_lshl_b64 s[10:11], s[44:45], 19
	s_add_u32 s20, s86, s10
	s_addc_u32 s21, s87, s11
	s_add_i32 s45, s54, 0
	v_lshl_or_b32 v192, v246, 11, v243
	s_add_i32 m0, s45, 0x10000
	v_lshl_or_b32 v194, v245, 11, v243
	global_load_lds_dwordx4 v192, s[20:21]
	s_add_i32 m0, s45, 0x12000
	s_add_u32 s10, s20, 0x40000
	global_load_lds_dwordx4 v194, s[20:21]
	s_addc_u32 s11, s21, 0
	s_add_i32 m0, s45, 0x14000
	s_add_i32 s55, s45, 0x2000
	global_load_lds_dwordx4 v192, s[10:11]
	s_add_i32 m0, s45, 0x16000
	s_add_i32 s56, s45, 0x4000
	global_load_lds_dwordx4 v194, s[10:11]
	s_mov_b32 m0, s45
	s_add_i32 s57, s45, 0x6000
	v_mov_b32_e32 v195, v193
	s_cmp_eq_u32 s3, 1
	v_lshl_add_u64 v[6:7], s[20:21], 0, v[192:193]
	v_lshl_add_u64 v[4:5], s[20:21], 0, v[194:195]
	v_mov_b32_e32 v199, v193
	s_cselect_b64 s[10:11], -1, 0
	s_cmp_lg_u32 s3, 1
	v_mov_b32_e32 v3, v193
	s_waitcnt vmcnt(0)
	v_lshl_or_b32 v198, v8, 11, v243
	v_lshl_or_b32 v2, v9, 11, v243
	global_load_lds_dwordx4 v198, s[40:41]
	s_mov_b32 m0, s55
	v_lshl_or_b32 v196, v10, 11, v243
	global_load_lds_dwordx4 v2, s[40:41]
	s_mov_b32 m0, s56
	v_lshl_or_b32 v0, v11, 11, v243
	global_load_lds_dwordx4 v196, s[40:41]
	s_mov_b32 m0, s57
	s_nop 0
	global_load_lds_dwordx4 v0, s[40:41]
	s_cbranch_scc1 .LBB0_801
	s_barrier

.LBB0_1013:
	s_mov_b32 s30, s98
	s_lshl_b32 s99, s98, 3
	s_nop 0
	v_writelane_b32 v253, s99, 19
	s_cmp_lt_i32 s90, 11
	s_cselect_b64 s[4:5], -1, 0
	s_and_b64 s[0:1], s[4:5], s[2:3]
	s_andn2_b64 vcc, exec, s[0:1]
	s_cbranch_vccnz .LBB0_1019
	s_abs_i32 s0, s78
	v_cvt_f32_u32_e32 v0, s0
	s_sub_i32 s1, s78, s94
	s_add_i32 s2, s1, 0x7fff
	s_sub_i32 s1, 0xffff8001, s1
	v_rcp_iflag_f32_e32 v0, v0
	s_xor_b32 s6, s2, s78
	s_sub_i32 s3, 0, s0
	s_max_i32 s1, s2, s1
	v_mul_f32_e32 v0, 0x4f7ffffe, v0
	v_cvt_u32_f32_e32 v0, v0
	s_ashr_i32 s2, s6, 31
	v_readfirstlane_b32 s6, v0
	s_mul_i32 s3, s3, s6
	s_mul_hi_u32 s3, s6, s3
	s_add_i32 s6, s6, s3
	s_mul_hi_u32 s3, s1, s6
	s_mul_i32 s6, s3, s0
	s_sub_i32 s1, s1, s6
	s_add_i32 s7, s3, 1
	s_sub_i32 s6, s1, s0
	s_cmp_ge_u32 s1, s0
	s_cselect_b32 s3, s7, s3
	s_cselect_b32 s1, s6, s1
	s_add_i32 s6, s3, 1
	s_cmp_ge_u32 s1, s0
	s_cselect_b32 s0, s6, s3
	s_xor_b32 s0, s0, s2
	s_sub_i32 s7, s0, s2
	s_cmp_lt_i32 s7, 1
	s_cbranch_scc1 .LBB0_1019
	s_add_u32 s8, s88, 0x6c00000
	s_addc_u32 s9, s89, 0
	s_add_u32 s10, s88, 0x510000
	s_addc_u32 s11, s89, 0
	s_add_i32 s0, s94, s78
	s_ashr_i32 s95, s94, 31
	s_min_i32 s2, s0, 0x7fff
	s_lshl_b64 s[0:1], s[94:95], 11
	s_add_u32 s0, s40, s0
	s_addc_u32 s1, s41, s1
	s_lshl_b32 s12, s94, 1
	s_ashr_i32 s13, s12, 31
	s_lshl_b64 s[12:13], s[12:13], 10
	s_add_u32 s12, s8, s12
	s_waitcnt vmcnt(0)
	v_lshlrev_b32_e32 v14, 2, v237
	s_addc_u32 s13, s9, s13
	v_lshlrev_b32_e32 v0, 3, v237
	global_load_dword v18, v14, s[12:13] offset:1792 nt
	global_load_dword v17, v14, s[12:13] offset:768 nt
	global_load_dword v20, v14, s[12:13] offset:1536 nt
	global_load_dword v24, v14, s[12:13] offset:1280 nt
	global_load_dword v26, v14, s[12:13] offset:1024 nt
	global_load_dword v21, v14, s[12:13] offset:512 nt
	global_load_dword v22, v14, s[12:13] offset:256 nt
	global_load_dword v23, v14, s[12:13] nt
	global_load_dwordx2 v[12:13], v0, s[0:1] offset:1536 nt
	global_load_dwordx2 v[10:11], v0, s[0:1] offset:1024 nt
	global_load_dwordx2 v[8:9], v0, s[0:1] offset:512 nt
	global_load_dwordx2 v[6:7], v0, s[0:1] nt
	v_mov_b32_e32 v1, 0
	v_lshl_add_u64 v[2:3], s[40:41], 0, v[0:1]
	v_lshl_add_u64 v[4:5], s[88:89], 0, v[0:1]
	v_mbcnt_lo_u32_b32 v0, -1, 0
	v_mbcnt_hi_u32_b32 v28, -1, v0
	v_and_b32_e32 v0, 64, v28
	s_mov_b64 s[0:1], 0x1b400000
	v_add_u32_e32 v29, 64, v0
	v_xor_b32_e32 v0, 1, v28
	v_lshl_add_u64 v[4:5], v[4:5], 0, s[0:1]
	v_cmp_lt_i32_e64 s[0:1], v0, v29
	v_xor_b32_e32 v16, 2, v28
	v_xor_b32_e32 v19, 4, v28
	v_cndmask_b32_e64 v0, v28, v0, s[0:1]
	v_cmp_lt_i32_e64 s[0:1], v16, v29
	v_xor_b32_e32 v25, 8, v28
	v_xor_b32_e32 v27, 16, v28
	v_cndmask_b32_e64 v16, v28, v16, s[0:1]
	v_cmp_lt_i32_e64 s[0:1], v19, v29
	v_xor_b32_e32 v30, 32, v28
	v_mov_b32_e32 v15, v1
	v_cndmask_b32_e64 v19, v28, v19, s[0:1]
	v_cmp_lt_i32_e64 s[0:1], v25, v29
	v_cmp_eq_u32_e32 vcc, 0, v237
	v_lshlrev_b32_e32 v0, 2, v0
	v_cndmask_b32_e64 v25, v28, v25, s[0:1]
	v_cmp_lt_i32_e64 s[0:1], v27, v29
	v_lshlrev_b32_e32 v16, 2, v16
	v_lshlrev_b32_e32 v19, 2, v19
	v_cndmask_b32_e64 v27, v28, v27, s[0:1]
	v_cmp_lt_i32_e64 s[0:1], v30, v29
	v_lshlrev_b32_e32 v25, 2, v25
	v_lshlrev_b32_e32 v27, 2, v27
	v_cndmask_b32_e64 v28, v28, v30, s[0:1]
	v_lshlrev_b32_e32 v28, 2, v28
	v_lshl_add_u64 v[14:15], s[8:9], 0, v[14:15]
	s_mov_b32 s6, 0x3d800000
	v_mov_b32_e32 v29, 0x358637bd
	s_mov_b32 s12, 0x800000
	s_branch .LBB0_1017

	.amdhsa_kernel _Z9hymba_fwd6Params
		.amdhsa_group_segment_fixed_size 0
		.amdhsa_private_segment_fixed_size 0
		.amdhsa_kernarg_size 512
		.amdhsa_user_sgpr_count 2
		.amdhsa_user_sgpr_dispatch_ptr 0
		.amdhsa_user_sgpr_queue_ptr 0
		.amdhsa_user_sgpr_kernarg_segment_ptr 1
		.amdhsa_user_sgpr_dispatch_id 0
		.amdhsa_user_sgpr_kernarg_preload_length 0
		.amdhsa_user_sgpr_kernarg_preload_offset 0
		.amdhsa_user_sgpr_private_segment_size 0
		.amdhsa_uses_dynamic_stack 0
		.amdhsa_enable_private_segment 0
		.amdhsa_system_sgpr_workgroup_id_x 1
		.amdhsa_system_sgpr_workgroup_id_y 0
		.amdhsa_system_sgpr_workgroup_id_z 0
		.amdhsa_system_sgpr_workgroup_info 0
		.amdhsa_system_vgpr_workitem_id 2
		.amdhsa_next_free_vgpr 254
		.amdhsa_next_free_sgpr 100
		.amdhsa_accum_offset 256
		.amdhsa_reserve_vcc 1
		.amdhsa_float_round_mode_32 0
		.amdhsa_float_round_mode_16_64 0
		.amdhsa_float_denorm_mode_32 3
		.amdhsa_float_denorm_mode_16_64 3
		.amdhsa_dx10_clamp 1
		.amdhsa_ieee_mode 1
		.amdhsa_fp16_overflow 0
		.amdhsa_tg_split 0
		.amdhsa_exception_fp_ieee_invalid_op 0
		.amdhsa_exception_fp_denorm_src 0
		.amdhsa_exception_fp_ieee_div_zero 0
		.amdhsa_exception_fp_ieee_overflow 0
		.amdhsa_exception_fp_ieee_underflow 0
		.amdhsa_exception_fp_ieee_inexact 0
		.amdhsa_exception_int_div_zero 0
	.end_amdhsa_kernel

amdhsa.kernels:
  - .agpr_count:     0
    .args:
      - .offset:         0
        .size:           256
        .value_kind:     by_value
      - .offset:         256
        .size:           4
        .value_kind:     hidden_block_count_x
      - .offset:         260
        .size:           4
        .value_kind:     hidden_block_count_y
      - .offset:         264
        .size:           4
        .value_kind:     hidden_block_count_z
      - .offset:         268
        .size:           2
        .value_kind:     hidden_group_size_x
      - .offset:         270
        .size:           2
        .value_kind:     hidden_group_size_y
      - .offset:         272
        .size:           2
        .value_kind:     hidden_group_size_z
      - .offset:         274
        .size:           2
        .value_kind:     hidden_remainder_x
      - .offset:         276
        .size:           2
        .value_kind:     hidden_remainder_y
      - .offset:         278
        .size:           2
        .value_kind:     hidden_remainder_z
      - .offset:         296
        .size:           8
        .value_kind:     hidden_global_offset_x
      - .offset:         304
        .size:           8
        .value_kind:     hidden_global_offset_y
      - .offset:         312
        .size:           8
        .value_kind:     hidden_global_offset_z
      - .offset:         320
        .size:           2
        .value_kind:     hidden_grid_dims
      - .offset:         344
        .size:           8
        .value_kind:     hidden_multigrid_sync_arg
      - .offset:         376
        .size:           4
        .value_kind:     hidden_dynamic_lds_size
    .group_segment_fixed_size: 0
    .kernarg_segment_align: 8
    .kernarg_segment_size: 512
    .language:       OpenCL C
    .language_version:
      - 2
      - 0
    .max_flat_workgroup_size: 512
    .name:           _Z9hymba_fwd6Params
    .private_segment_fixed_size: 0
    .sgpr_count:     106
    .sgpr_spill_count: 57
    .symbol:         _Z9hymba_fwd6Params.kd
    .uniform_work_group_size: 1
    .uses_dynamic_stack: false
    .vgpr_count:     254
    .vgpr_spill_count: 0
    .wavefront_size: 64
